# speedup vs baseline: 1.0240x; 1.0240x over previous
.LBB0_44:
	v_ashrrev_i32_e32 v3, 31, v2
	v_lshl_add_u64 v[2:3], v[2:3], 2, s[22:23]
	v_or_b32_e32 v1, 7, v4
	global_store_dword v[2:3], v1, off
	s_or_b64 exec, exec, s[6:7]
	s_and_saveexec_b64 s[4:5], s[20:21]
	s_cbranch_execnz .LBB0_29
	s_branch .LBB0_30
	.p2align	8

.LBB1_245:
	s_endpgm
	.p2align	8

_ZN12_GLOBAL__N_112oproj_kernelEPKDF16_S1_PKfPf:
	s_load_dwordx8 s[4:11], s[0:1], 0x0
	s_lshl_b32 s1, s2, 4
	s_and_b32 s3, s1, 0x180
	s_lshr_b32 s1, s2, 2
	s_and_b32 s0, s2, 7
	s_and_b32 s1, s1, 0x1fffff8
	s_or_b32 s0, s1, s0
	s_lshl_b32 s0, s0, 7
	s_mov_b32 s1, 0
	s_lshl_b64 s[12:13], s[0:1], 10
	v_lshrrev_b32_e32 v36, 3, v0
	s_waitcnt lgkmcnt(0)
	s_add_u32 s4, s4, s12
	s_addc_u32 s5, s5, s13
	v_lshlrev_b32_e32 v238, 10, v36
	v_mov_b32_e32 v239, 0
	v_lshlrev_b32_e32 v37, 4, v0
	v_lshl_add_u64 v[2:3], s[4:5], 0, v[238:239]
	v_and_b32_e32 v238, 0x70, v37
	v_lshl_add_u64 v[66:67], v[2:3], 0, v[238:239]
	s_mov_b32 s1, 0x8000
	v_add_co_u32_e32 v68, vcc, s1, v66
	s_mov_b32 s2, 0x10000
	s_nop 0
	v_addc_co_u32_e32 v69, vcc, 0, v67, vcc
	v_add_co_u32_e32 v70, vcc, s2, v66
	v_or_b32_e32 v1, s3, v36
	s_nop 0
	v_addc_co_u32_e32 v71, vcc, 0, v67, vcc
	s_mov_b32 s4, 0x18000
	v_add_co_u32_e32 v72, vcc, s4, v66
	v_lshl_add_u64 v[18:19], s[6:7], 0, v[238:239]
	v_lshlrev_b32_e32 v34, 10, v1
	v_mov_b32_e32 v35, v239
	v_addc_co_u32_e32 v73, vcc, 0, v67, vcc
	v_lshl_add_u64 v[74:75], v[18:19], 0, v[34:35]
	v_add_co_u32_e32 v76, vcc, s1, v74
	global_load_dwordx4 v[2:5], v[66:67], off
	global_load_dwordx4 v[6:9], v[68:69], off
	v_addc_co_u32_e32 v77, vcc, 0, v75, vcc
	v_add_co_u32_e32 v78, vcc, s2, v74
	global_load_dwordx4 v[10:13], v[70:71], off
	global_load_dwordx4 v[14:17], v[72:73], off
	v_addc_co_u32_e32 v79, vcc, 0, v75, vcc
	v_add_co_u32_e32 v80, vcc, s4, v74
	global_load_dwordx4 v[18:21], v[74:75], off
	global_load_dwordx4 v[22:25], v[76:77], off
	v_addc_co_u32_e32 v81, vcc, 0, v75, vcc
	global_load_dwordx4 v[26:29], v[78:79], off
	global_load_dwordx4 v[30:33], v[80:81], off
	v_lshl_add_u64 v[34:35], s[6:7], 0, v[34:35]
	s_movk_i32 s5, 0x70
	v_xor_b32_e32 v37, v37, v0
	v_lshlrev_b32_e32 v36, 7, v36
	v_lshl_add_u64 v[34:35], v[34:35], 0, v[238:239]
	v_and_or_b32 v82, v37, s5, v36
	v_add_co_u32_e32 v36, vcc, s1, v34
	global_load_dwordx4 v[100:103], v[66:67], off offset:128
	global_load_dwordx4 v[104:107], v[68:69], off offset:128
	global_load_dwordx4 v[112:115], v[70:71], off offset:128
	global_load_dwordx4 v[116:119], v[72:73], off offset:128
	v_addc_co_u32_e32 v37, vcc, 0, v35, vcc
	global_load_dwordx4 v[120:123], v[34:35], off offset:128
	global_load_dwordx4 v[124:127], v[36:37], off offset:128
	v_add_co_u32_e32 v36, vcc, s2, v34
	v_lshrrev_b32_e32 v1, 1, v0
	s_nop 0
	v_addc_co_u32_e32 v37, vcc, 0, v35, vcc
	v_add_co_u32_e32 v34, vcc, s4, v34
	v_lshrrev_b32_e32 v38, 5, v0
	s_nop 0
	v_addc_co_u32_e32 v35, vcc, 0, v35, vcc
	global_load_dwordx4 v[128:131], v[36:37], off offset:128
	global_load_dwordx4 v[132:135], v[34:35], off offset:128
	v_and_b32_e32 v1, 64, v1
	v_bfe_u32 v144, v0, 1, 3
	v_and_or_b32 v39, v0, 31, v1
	v_lshlrev_b32_e32 v87, 7, v39
	v_bfe_u32 v240, v0, 5, 1
	v_bitop3_b32 v85, v240, v144, 2 bitop3:0x36
	v_lshlrev_b32_e32 v86, 4, v85
	v_or_b32_e32 v85, v87, v86
	v_mov_b32_e32 v241, v239
	s_waitcnt vmcnt(15)
	ds_write_b128 v82, v[2:5]
	s_waitcnt vmcnt(14)
	ds_write_b128 v82, v[6:9] offset:4096
	s_waitcnt vmcnt(13)
	ds_write_b128 v82, v[10:13] offset:8192
	s_waitcnt vmcnt(12)
	ds_write_b128 v82, v[14:17] offset:12288
	s_waitcnt vmcnt(11)
	ds_write_b128 v82, v[18:21] offset:16384
	s_waitcnt vmcnt(10)
	ds_write_b128 v82, v[22:25] offset:20480
	s_waitcnt vmcnt(9)
	ds_write_b128 v82, v[26:29] offset:24576
	s_waitcnt vmcnt(8)
	ds_write_b128 v82, v[30:33] offset:28672
	v_bitop3_b32 v2, v38, v144, 1 bitop3:0x6c
	v_lshlrev_b32_e32 v6, 4, v2
	v_or_b32_e32 v83, v87, v6
	s_waitcnt lgkmcnt(0)
	s_barrier
	ds_read_b128 v[2:5], v83
	v_lshlrev_b32_e32 v7, 7, v0
	v_and_b32_e32 v145, 0x2f80, v7
	v_or_b32_e32 v84, v145, v6
	ds_read_b128 v[6:9], v84 offset:16384
	ds_read_b128 v[10:13], v83 offset:4096
	ds_read_b128 v[14:17], v84 offset:20480
	ds_read_b128 v[88:91], v85
	s_waitcnt lgkmcnt(3)
	v_mfma_f32_32x32x16_f16 v[50:65], v[2:5], v[6:9], 0
	v_or_b32_e32 v86, v145, v86
	ds_read_b128 v[92:95], v86 offset:16384
	ds_read_b128 v[96:99], v85 offset:4096
	ds_read_b128 v[108:111], v86 offset:20480
	v_and_b32_e32 v0, 0x5f, v0
	v_or_b32_e32 v0, s3, v0
	v_lshlrev_b32_e32 v238, 2, v0
	v_lshlrev_b32_e32 v0, 2, v240
	s_waitcnt lgkmcnt(4)
	v_mfma_f32_32x32x16_f16 v[18:33], v[2:5], v[14:17], 0
	v_mfma_f32_32x32x16_f16 v[34:49], v[10:13], v[6:9], 0
	v_mfma_f32_32x32x16_f16 v[2:17], v[10:13], v[14:17], 0
	s_waitcnt lgkmcnt(2)
	v_mfma_f32_32x32x16_f16 v[50:65], v[88:91], v[92:95], v[50:65]
	s_waitcnt lgkmcnt(0)
	v_mfma_f32_32x32x16_f16 v[18:33], v[88:91], v[108:111], v[18:33]
	v_bitop3_b32 v88, v240, v144, 4 bitop3:0x36
	v_lshlrev_b32_e32 v88, 4, v88
	v_or_b32_e32 v90, v87, v88
	v_mfma_f32_32x32x16_f16 v[34:49], v[96:99], v[92:95], v[34:49]
	v_or_b32_e32 v94, v145, v88
	v_bitop3_b32 v88, v240, v144, 6 bitop3:0x36
	v_lshlrev_b32_e32 v88, 4, v88
	v_or3_b32 v240, s0, v1, v0
	v_lshl_add_u64 v[0:1], s[10:11], 0, v[238:239]
	v_mfma_f32_32x32x16_f16 v[2:17], v[96:99], v[108:111], v[2:17]
	ds_read_b128 v[96:99], v90
	ds_read_b128 v[108:111], v94 offset:16384
	ds_read_b128 v[136:139], v90 offset:4096
	ds_read_b128 v[140:143], v94 offset:20480
	s_waitcnt lgkmcnt(2)
	v_mfma_f32_32x32x16_f16 v[50:65], v[96:99], v[108:111], v[50:65]
	s_waitcnt lgkmcnt(0)
	v_mfma_f32_32x32x16_f16 v[18:33], v[96:99], v[140:143], v[18:33]
	v_or_b32_e32 v98, v87, v88
	v_mfma_f32_32x32x16_f16 v[34:49], v[136:139], v[108:111], v[34:49]
	v_or_b32_e32 v110, v145, v88
	v_mfma_f32_32x32x16_f16 v[2:17], v[136:139], v[140:143], v[2:17]
	ds_read_b128 v[136:139], v98
	ds_read_b128 v[140:143], v110 offset:16384
	ds_read_b128 v[144:147], v98 offset:4096
	ds_read_b128 v[148:151], v110 offset:20480
	s_waitcnt lgkmcnt(2)
	v_mfma_f32_32x32x16_f16 v[50:65], v[136:139], v[140:143], v[50:65]
	s_waitcnt lgkmcnt(0)
	v_mfma_f32_32x32x16_f16 v[18:33], v[136:139], v[148:151], v[18:33]
	v_mfma_f32_32x32x16_f16 v[34:49], v[144:147], v[140:143], v[34:49]
	global_load_dwordx4 v[136:139], v[66:67], off offset:256
	global_load_dwordx4 v[140:143], v[68:69], off offset:256
	global_load_dwordx4 v[152:155], v[70:71], off offset:256
	global_load_dwordx4 v[156:159], v[72:73], off offset:256
	global_load_dwordx4 v[160:163], v[74:75], off offset:256
	global_load_dwordx4 v[164:167], v[76:77], off offset:256
	global_load_dwordx4 v[168:171], v[78:79], off offset:256
	global_load_dwordx4 v[172:175], v[80:81], off offset:256
	s_waitcnt vmcnt(15)
	ds_write_b128 v82, v[100:103] offset:32768
	s_waitcnt vmcnt(14)
	ds_write_b128 v82, v[104:107] offset:36864
	s_waitcnt vmcnt(13)
	ds_write_b128 v82, v[112:115] offset:40960
	s_waitcnt vmcnt(12)
	ds_write_b128 v82, v[116:119] offset:45056
	s_waitcnt vmcnt(11)
	ds_write_b128 v82, v[120:123] offset:49152
	s_waitcnt vmcnt(10)
	ds_write_b128 v82, v[124:127] offset:53248
	s_waitcnt vmcnt(9)
	ds_write_b128 v82, v[128:131] offset:57344
	s_waitcnt vmcnt(8)
	ds_write_b128 v82, v[132:135] offset:61440
	s_waitcnt lgkmcnt(0)
	s_barrier
	ds_read_b128 v[100:103], v83 offset:32768
	ds_read_b128 v[104:107], v84 offset:49152
	ds_read_b128 v[112:115], v83 offset:36864
	ds_read_b128 v[116:119], v84 offset:53248
	v_mfma_f32_32x32x16_f16 v[2:17], v[144:147], v[148:151], v[2:17]
	s_waitcnt lgkmcnt(2)
	v_mfma_f32_32x32x16_f16 v[50:65], v[100:103], v[104:107], v[50:65]
	s_waitcnt lgkmcnt(0)
	v_mfma_f32_32x32x16_f16 v[18:33], v[100:103], v[116:119], v[18:33]
	v_mfma_f32_32x32x16_f16 v[34:49], v[112:115], v[104:107], v[34:49]
	v_mfma_f32_32x32x16_f16 v[2:17], v[112:115], v[116:119], v[2:17]
	ds_read_b128 v[100:103], v85 offset:32768
	ds_read_b128 v[104:107], v86 offset:49152
	ds_read_b128 v[112:115], v85 offset:36864
	ds_read_b128 v[116:119], v86 offset:53248
	s_waitcnt lgkmcnt(2)
	v_mfma_f32_32x32x16_f16 v[50:65], v[100:103], v[104:107], v[50:65]
	s_waitcnt lgkmcnt(0)
	v_mfma_f32_32x32x16_f16 v[18:33], v[100:103], v[116:119], v[18:33]
	v_mfma_f32_32x32x16_f16 v[34:49], v[112:115], v[104:107], v[34:49]
	v_mfma_f32_32x32x16_f16 v[2:17], v[112:115], v[116:119], v[2:17]
	ds_read_b128 v[100:103], v90 offset:32768
	ds_read_b128 v[104:107], v94 offset:49152
	ds_read_b128 v[112:115], v90 offset:36864
	ds_read_b128 v[116:119], v94 offset:53248
	s_waitcnt lgkmcnt(2)
	v_mfma_f32_32x32x16_f16 v[50:65], v[100:103], v[104:107], v[50:65]
	s_waitcnt lgkmcnt(0)
	v_mfma_f32_32x32x16_f16 v[18:33], v[100:103], v[116:119], v[18:33]
	v_mfma_f32_32x32x16_f16 v[34:49], v[112:115], v[104:107], v[34:49]
	v_mfma_f32_32x32x16_f16 v[2:17], v[112:115], v[116:119], v[2:17]
	ds_read_b128 v[100:103], v98 offset:32768
	ds_read_b128 v[104:107], v110 offset:49152
	ds_read_b128 v[112:115], v98 offset:36864
	ds_read_b128 v[116:119], v110 offset:53248
	s_waitcnt lgkmcnt(2)
	v_mfma_f32_32x32x16_f16 v[50:65], v[100:103], v[104:107], v[50:65]
	s_waitcnt lgkmcnt(0)
	v_mfma_f32_32x32x16_f16 v[18:33], v[100:103], v[116:119], v[18:33]
	v_mfma_f32_32x32x16_f16 v[34:49], v[112:115], v[104:107], v[34:49]
	global_load_dwordx4 v[100:103], v[66:67], off offset:384
	global_load_dwordx4 v[104:107], v[68:69], off offset:384
	global_load_dwordx4 v[120:123], v[70:71], off offset:384
	global_load_dwordx4 v[124:127], v[72:73], off offset:384
	global_load_dwordx4 v[128:131], v[74:75], off offset:384
	global_load_dwordx4 v[132:135], v[76:77], off offset:384
	global_load_dwordx4 v[144:147], v[78:79], off offset:384
	global_load_dwordx4 v[148:151], v[80:81], off offset:384
	s_waitcnt vmcnt(15)
	ds_write_b128 v82, v[136:139]
	s_waitcnt vmcnt(14)
	ds_write_b128 v82, v[140:143] offset:4096
	s_waitcnt vmcnt(13)
	ds_write_b128 v82, v[152:155] offset:8192
	s_waitcnt vmcnt(12)
	ds_write_b128 v82, v[156:159] offset:12288
	s_waitcnt vmcnt(11)
	ds_write_b128 v82, v[160:163] offset:16384
	s_waitcnt vmcnt(10)
	ds_write_b128 v82, v[164:167] offset:20480
	s_waitcnt vmcnt(9)
	ds_write_b128 v82, v[168:171] offset:24576
	s_waitcnt vmcnt(8)
	ds_write_b128 v82, v[172:175] offset:28672
	s_waitcnt lgkmcnt(0)
	s_barrier
	v_mfma_f32_32x32x16_f16 v[2:17], v[112:115], v[116:119], v[2:17]
	ds_read_b128 v[112:115], v83
	ds_read_b128 v[116:119], v84 offset:16384
	ds_read_b128 v[136:139], v83 offset:4096
	ds_read_b128 v[140:143], v84 offset:20480
	s_waitcnt lgkmcnt(2)
	v_mfma_f32_32x32x16_f16 v[50:65], v[112:115], v[116:119], v[50:65]
	s_waitcnt lgkmcnt(0)
	v_mfma_f32_32x32x16_f16 v[18:33], v[112:115], v[140:143], v[18:33]
	v_mfma_f32_32x32x16_f16 v[34:49], v[136:139], v[116:119], v[34:49]
	v_mfma_f32_32x32x16_f16 v[2:17], v[136:139], v[140:143], v[2:17]
	ds_read_b128 v[112:115], v85
	ds_read_b128 v[116:119], v86 offset:16384
	ds_read_b128 v[136:139], v85 offset:4096
	ds_read_b128 v[140:143], v86 offset:20480
	s_waitcnt lgkmcnt(2)
	v_mfma_f32_32x32x16_f16 v[50:65], v[112:115], v[116:119], v[50:65]
	s_waitcnt lgkmcnt(0)
	v_mfma_f32_32x32x16_f16 v[18:33], v[112:115], v[140:143], v[18:33]
	v_mfma_f32_32x32x16_f16 v[34:49], v[136:139], v[116:119], v[34:49]
	v_mfma_f32_32x32x16_f16 v[2:17], v[136:139], v[140:143], v[2:17]
	ds_read_b128 v[112:115], v90
	ds_read_b128 v[116:119], v94 offset:16384
	ds_read_b128 v[136:139], v90 offset:4096
	ds_read_b128 v[140:143], v94 offset:20480
	s_waitcnt lgkmcnt(2)
	v_mfma_f32_32x32x16_f16 v[50:65], v[112:115], v[116:119], v[50:65]
	s_waitcnt lgkmcnt(0)
	v_mfma_f32_32x32x16_f16 v[18:33], v[112:115], v[140:143], v[18:33]
	v_mfma_f32_32x32x16_f16 v[34:49], v[136:139], v[116:119], v[34:49]
	v_mfma_f32_32x32x16_f16 v[2:17], v[136:139], v[140:143], v[2:17]
	ds_read_b128 v[112:115], v98
	ds_read_b128 v[116:119], v110 offset:16384
	ds_read_b128 v[136:139], v98 offset:4096
	ds_read_b128 v[140:143], v110 offset:20480
	s_waitcnt lgkmcnt(2)
	v_mfma_f32_32x32x16_f16 v[50:65], v[112:115], v[116:119], v[50:65]
	s_waitcnt lgkmcnt(0)
	v_mfma_f32_32x32x16_f16 v[18:33], v[112:115], v[140:143], v[18:33]
	v_mfma_f32_32x32x16_f16 v[34:49], v[136:139], v[116:119], v[34:49]
	global_load_dwordx4 v[112:115], v[66:67], off offset:512
	global_load_dwordx4 v[116:119], v[68:69], off offset:512
	global_load_dwordx4 v[152:155], v[70:71], off offset:512
	global_load_dwordx4 v[156:159], v[72:73], off offset:512
	global_load_dwordx4 v[160:163], v[74:75], off offset:512
	global_load_dwordx4 v[164:167], v[76:77], off offset:512
	global_load_dwordx4 v[168:171], v[78:79], off offset:512
	global_load_dwordx4 v[172:175], v[80:81], off offset:512
	s_waitcnt vmcnt(15)
	ds_write_b128 v82, v[100:103] offset:32768
	s_waitcnt vmcnt(14)
	ds_write_b128 v82, v[104:107] offset:36864
	s_waitcnt vmcnt(13)
	ds_write_b128 v82, v[120:123] offset:40960
	s_waitcnt vmcnt(12)
	ds_write_b128 v82, v[124:127] offset:45056
	s_waitcnt vmcnt(11)
	ds_write_b128 v82, v[128:131] offset:49152
	s_waitcnt vmcnt(10)
	ds_write_b128 v82, v[132:135] offset:53248
	s_waitcnt vmcnt(9)
	ds_write_b128 v82, v[144:147] offset:57344
	s_waitcnt vmcnt(8)
	ds_write_b128 v82, v[148:151] offset:61440
	s_waitcnt lgkmcnt(0)
	s_barrier
	ds_read_b128 v[100:103], v83 offset:32768
	ds_read_b128 v[104:107], v84 offset:49152
	ds_read_b128 v[120:123], v83 offset:36864
	ds_read_b128 v[124:127], v84 offset:53248
	v_mfma_f32_32x32x16_f16 v[2:17], v[136:139], v[140:143], v[2:17]
	s_waitcnt lgkmcnt(2)
	v_mfma_f32_32x32x16_f16 v[50:65], v[100:103], v[104:107], v[50:65]
	s_waitcnt lgkmcnt(0)
	v_mfma_f32_32x32x16_f16 v[18:33], v[100:103], v[124:127], v[18:33]
	v_mfma_f32_32x32x16_f16 v[34:49], v[120:123], v[104:107], v[34:49]
	v_mfma_f32_32x32x16_f16 v[2:17], v[120:123], v[124:127], v[2:17]
	ds_read_b128 v[100:103], v85 offset:32768
	ds_read_b128 v[104:107], v86 offset:49152
	ds_read_b128 v[120:123], v85 offset:36864
	ds_read_b128 v[124:127], v86 offset:53248
	s_waitcnt lgkmcnt(2)
	v_mfma_f32_32x32x16_f16 v[50:65], v[100:103], v[104:107], v[50:65]
	s_waitcnt lgkmcnt(0)
	v_mfma_f32_32x32x16_f16 v[18:33], v[100:103], v[124:127], v[18:33]
	v_mfma_f32_32x32x16_f16 v[34:49], v[120:123], v[104:107], v[34:49]
	v_mfma_f32_32x32x16_f16 v[2:17], v[120:123], v[124:127], v[2:17]
	ds_read_b128 v[100:103], v90 offset:32768
	ds_read_b128 v[104:107], v94 offset:49152
	ds_read_b128 v[120:123], v90 offset:36864
	ds_read_b128 v[124:127], v94 offset:53248
	s_waitcnt lgkmcnt(2)
	v_mfma_f32_32x32x16_f16 v[50:65], v[100:103], v[104:107], v[50:65]
	s_waitcnt lgkmcnt(0)
	v_mfma_f32_32x32x16_f16 v[18:33], v[100:103], v[124:127], v[18:33]
	v_mfma_f32_32x32x16_f16 v[34:49], v[120:123], v[104:107], v[34:49]
	v_mfma_f32_32x32x16_f16 v[2:17], v[120:123], v[124:127], v[2:17]
	ds_read_b128 v[100:103], v98 offset:32768
	ds_read_b128 v[104:107], v110 offset:49152
	ds_read_b128 v[120:123], v98 offset:36864
	ds_read_b128 v[124:127], v110 offset:53248
	s_waitcnt lgkmcnt(2)
	v_mfma_f32_32x32x16_f16 v[50:65], v[100:103], v[104:107], v[50:65]
	s_waitcnt lgkmcnt(0)
	v_mfma_f32_32x32x16_f16 v[18:33], v[100:103], v[124:127], v[18:33]
	v_mfma_f32_32x32x16_f16 v[34:49], v[120:123], v[104:107], v[34:49]
	global_load_dwordx4 v[100:103], v[66:67], off offset:640
	global_load_dwordx4 v[104:107], v[68:69], off offset:640
	global_load_dwordx4 v[128:131], v[70:71], off offset:640
	global_load_dwordx4 v[132:135], v[72:73], off offset:640
	global_load_dwordx4 v[136:139], v[74:75], off offset:640
	global_load_dwordx4 v[140:143], v[76:77], off offset:640
	global_load_dwordx4 v[144:147], v[78:79], off offset:640
	global_load_dwordx4 v[148:151], v[80:81], off offset:640
	s_waitcnt vmcnt(15)
	ds_write_b128 v82, v[112:115]
	s_waitcnt vmcnt(14)
	ds_write_b128 v82, v[116:119] offset:4096
	s_waitcnt vmcnt(13)
	ds_write_b128 v82, v[152:155] offset:8192
	s_waitcnt vmcnt(12)
	ds_write_b128 v82, v[156:159] offset:12288
	s_waitcnt vmcnt(11)
	ds_write_b128 v82, v[160:163] offset:16384
	s_waitcnt vmcnt(10)
	ds_write_b128 v82, v[164:167] offset:20480
	s_waitcnt vmcnt(9)
	ds_write_b128 v82, v[168:171] offset:24576
	s_waitcnt vmcnt(8)
	ds_write_b128 v82, v[172:175] offset:28672
	s_waitcnt lgkmcnt(0)
	s_barrier
	v_mfma_f32_32x32x16_f16 v[2:17], v[120:123], v[124:127], v[2:17]
	ds_read_b128 v[112:115], v83
	ds_read_b128 v[116:119], v84 offset:16384
	ds_read_b128 v[120:123], v83 offset:4096
	ds_read_b128 v[124:127], v84 offset:20480
	s_waitcnt lgkmcnt(2)
	v_mfma_f32_32x32x16_f16 v[50:65], v[112:115], v[116:119], v[50:65]
	s_waitcnt lgkmcnt(0)
	v_mfma_f32_32x32x16_f16 v[18:33], v[112:115], v[124:127], v[18:33]
	v_mfma_f32_32x32x16_f16 v[34:49], v[120:123], v[116:119], v[34:49]
	v_mfma_f32_32x32x16_f16 v[2:17], v[120:123], v[124:127], v[2:17]
	ds_read_b128 v[112:115], v85
	ds_read_b128 v[116:119], v86 offset:16384
	ds_read_b128 v[120:123], v85 offset:4096
	ds_read_b128 v[124:127], v86 offset:20480
	s_waitcnt lgkmcnt(2)
	v_mfma_f32_32x32x16_f16 v[50:65], v[112:115], v[116:119], v[50:65]
	s_waitcnt lgkmcnt(0)
	v_mfma_f32_32x32x16_f16 v[18:33], v[112:115], v[124:127], v[18:33]
	v_mfma_f32_32x32x16_f16 v[34:49], v[120:123], v[116:119], v[34:49]
	v_mfma_f32_32x32x16_f16 v[2:17], v[120:123], v[124:127], v[2:17]
	ds_read_b128 v[112:115], v90
	ds_read_b128 v[116:119], v94 offset:16384
	ds_read_b128 v[120:123], v90 offset:4096
	ds_read_b128 v[124:127], v94 offset:20480
	s_waitcnt lgkmcnt(2)
	v_mfma_f32_32x32x16_f16 v[50:65], v[112:115], v[116:119], v[50:65]
	s_waitcnt lgkmcnt(0)
	v_mfma_f32_32x32x16_f16 v[18:33], v[112:115], v[124:127], v[18:33]
	v_mfma_f32_32x32x16_f16 v[34:49], v[120:123], v[116:119], v[34:49]
	v_mfma_f32_32x32x16_f16 v[2:17], v[120:123], v[124:127], v[2:17]
	ds_read_b128 v[112:115], v98
	ds_read_b128 v[116:119], v110 offset:16384
	ds_read_b128 v[120:123], v98 offset:4096
	ds_read_b128 v[124:127], v110 offset:20480
	global_load_dwordx4 v[152:155], v[66:67], off offset:768
	global_load_dwordx4 v[156:159], v[68:69], off offset:768
	global_load_dwordx4 v[160:163], v[70:71], off offset:768
	global_load_dwordx4 v[164:167], v[72:73], off offset:768
	global_load_dwordx4 v[168:171], v[74:75], off offset:768
	global_load_dwordx4 v[172:175], v[76:77], off offset:768
	global_load_dwordx4 v[176:179], v[78:79], off offset:768
	global_load_dwordx4 v[206:209], v[80:81], off offset:768
	s_waitcnt vmcnt(15)
	ds_write_b128 v82, v[100:103] offset:32768
	s_waitcnt vmcnt(14)
	ds_write_b128 v82, v[104:107] offset:36864
	s_waitcnt vmcnt(13)
	ds_write_b128 v82, v[128:131] offset:40960
	s_waitcnt vmcnt(12)
	ds_write_b128 v82, v[132:135] offset:45056
	s_waitcnt vmcnt(11)
	ds_write_b128 v82, v[136:139] offset:49152
	s_waitcnt vmcnt(10)
	ds_write_b128 v82, v[140:143] offset:53248
	s_waitcnt vmcnt(9)
	ds_write_b128 v82, v[144:147] offset:57344
	s_waitcnt vmcnt(8)
	ds_write_b128 v82, v[148:151] offset:61440
	s_waitcnt lgkmcnt(0)
	s_barrier
	v_mfma_f32_32x32x16_f16 v[50:65], v[112:115], v[116:119], v[50:65]
	v_mfma_f32_32x32x16_f16 v[18:33], v[112:115], v[124:127], v[18:33]
	v_mfma_f32_32x32x16_f16 v[34:49], v[120:123], v[116:119], v[34:49]
	ds_read_b128 v[100:103], v83 offset:32768
	ds_read_b128 v[104:107], v84 offset:49152
	ds_read_b128 v[112:115], v83 offset:36864
	ds_read_b128 v[116:119], v84 offset:53248
	global_load_dwordx4 v[222:225], v[66:67], off offset:896
	global_load_dwordx4 v[226:229], v[68:69], off offset:896
	ds_read_b128 v[66:69], v85 offset:32768
	global_load_dwordx4 v[230:233], v[70:71], off offset:896
	global_load_dwordx4 v[234:237], v[72:73], off offset:896
	ds_read_b128 v[202:205], v86 offset:49152
	global_load_dwordx4 v[242:245], v[74:75], off offset:896
	s_nop 0
	global_load_dwordx4 v[74:77], v[76:77], off offset:896
	ds_read_b128 v[186:189], v85 offset:36864
	ds_read_b128 v[190:193], v86 offset:53248
	global_load_dwordx4 v[246:249], v[78:79], off offset:896
	s_nop 0
	global_load_dwordx4 v[78:81], v[80:81], off offset:896
	s_waitcnt lgkmcnt(6)
	v_mfma_f32_32x32x16_f16 v[50:65], v[100:103], v[104:107], v[50:65]
	v_mfma_f32_32x32x16_f16 v[2:17], v[120:123], v[124:127], v[2:17]
	s_waitcnt lgkmcnt(4)
	v_mfma_f32_32x32x16_f16 v[18:33], v[100:103], v[116:119], v[18:33]
	s_waitcnt lgkmcnt(2)
	v_mfma_f32_32x32x16_f16 v[50:65], v[66:69], v[202:205], v[50:65]
	v_mfma_f32_32x32x16_f16 v[34:49], v[112:115], v[104:107], v[34:49]
	v_mfma_f32_32x32x16_f16 v[2:17], v[112:115], v[116:119], v[2:17]
	ds_read_b128 v[198:201], v90 offset:32768
	ds_read_b128 v[114:117], v90 offset:36864
	ds_read_b128 v[182:185], v94 offset:49152
	ds_read_b128 v[122:125], v94 offset:53248
	ds_read_b128 v[130:133], v98 offset:32768
	ds_read_b128 v[102:105], v98 offset:36864
	ds_read_b128 v[194:197], v110 offset:49152
	ds_read_b128 v[106:109], v110 offset:53248
	s_waitcnt vmcnt(15)
	ds_write_b128 v82, v[152:155]
	s_waitcnt vmcnt(14)
	ds_write_b128 v82, v[156:159] offset:4096
	s_waitcnt vmcnt(13)
	ds_write_b128 v82, v[160:163] offset:8192
	s_waitcnt vmcnt(12)
	ds_write_b128 v82, v[164:167] offset:12288
	s_waitcnt lgkmcnt(12)
	v_mfma_f32_32x32x16_f16 v[18:33], v[66:69], v[190:193], v[18:33]
	s_waitcnt vmcnt(11)
	ds_write_b128 v82, v[168:171] offset:16384
	s_waitcnt vmcnt(10)
	ds_write_b128 v82, v[172:175] offset:20480
	s_waitcnt vmcnt(9)
	ds_write_b128 v82, v[176:179] offset:24576
	s_waitcnt vmcnt(8)
	ds_write_b128 v82, v[206:209] offset:28672
	s_waitcnt lgkmcnt(0)
	s_barrier
	ds_read_b128 v[162:165], v83
	ds_read_b128 v[206:209], v84 offset:16384
	ds_read_b128 v[150:153], v83 offset:4096
	ds_read_b128 v[154:157], v84 offset:20480
	ds_read_b128 v[158:161], v85
	ds_read_b128 v[134:137], v85 offset:4096
	ds_read_b128 v[210:213], v86 offset:16384
	ds_read_b128 v[142:145], v86 offset:20480
	ds_read_b128 v[146:149], v90
	ds_read_b128 v[118:121], v90 offset:4096
	ds_read_b128 v[214:217], v94 offset:16384
	ds_read_b128 v[126:129], v94 offset:20480
	ds_read_b128 v[138:141], v98
	ds_read_b128 v[66:69], v98 offset:4096
	ds_read_b128 v[218:221], v110 offset:16384
	ds_read_b128 v[70:73], v110 offset:20480
	v_mfma_f32_32x32x16_f16 v[50:65], v[198:201], v[182:185], v[50:65]
	s_waitcnt vmcnt(7)
	ds_write_b128 v82, v[222:225] offset:32768
	s_waitcnt vmcnt(6)
	ds_write_b128 v82, v[226:229] offset:36864
	s_waitcnt vmcnt(5)
	ds_write_b128 v82, v[230:233] offset:40960
	s_waitcnt vmcnt(4)
	ds_write_b128 v82, v[234:237] offset:45056
	s_waitcnt vmcnt(3)
	ds_write_b128 v82, v[242:245] offset:49152
	s_waitcnt vmcnt(2)
	ds_write_b128 v82, v[74:77] offset:53248
	s_waitcnt vmcnt(1)
	ds_write_b128 v82, v[246:249] offset:57344
	s_waitcnt vmcnt(0)
	ds_write_b128 v82, v[78:81] offset:61440
	s_waitcnt lgkmcnt(0)
	s_barrier
	ds_read_b128 v[166:169], v83 offset:32768
	ds_read_b128 v[222:225], v84 offset:49152
	ds_read_b128 v[74:77], v83 offset:36864
	ds_read_b128 v[78:81], v84 offset:53248
	ds_read_b128 v[170:173], v85 offset:32768
	ds_read_b128 v[82:85], v85 offset:36864
	ds_read_b128 v[226:229], v86 offset:49152
	ds_read_b128 v[86:89], v86 offset:53248
	ds_read_b128 v[174:177], v90 offset:32768
	ds_read_b128 v[90:93], v90 offset:36864
	ds_read_b128 v[230:233], v94 offset:49152
	ds_read_b128 v[94:97], v94 offset:53248
	ds_read_b128 v[178:181], v98 offset:32768
	ds_read_b128 v[98:101], v98 offset:36864
	ds_read_b128 v[234:237], v110 offset:49152
	ds_read_b128 v[110:113], v110 offset:53248
	s_waitcnt lgkmcnt(0)
	s_barrier
	global_load_dword v244, v238, s[8:9]
	global_load_dword v245, v238, s[8:9] offset:128
	v_mfma_f32_32x32x16_f16 v[50:65], v[130:133], v[194:197], v[50:65]
	v_lshlrev_b64 v[242:243], 11, v[240:241]
	v_lshl_add_u64 v[242:243], v[0:1], 0, v[242:243]
	v_or_b32_e32 v238, 59, v240
	v_mfma_f32_32x32x16_f16 v[50:65], v[162:165], v[206:209], v[50:65]
	v_mfma_f32_32x32x16_f16 v[50:65], v[158:161], v[210:213], v[50:65]
	v_mfma_f32_32x32x16_f16 v[50:65], v[146:149], v[214:217], v[50:65]
	v_mfma_f32_32x32x16_f16 v[50:65], v[138:141], v[218:221], v[50:65]
	v_mfma_f32_32x32x16_f16 v[34:49], v[186:189], v[202:205], v[34:49]
	v_mov_b32_e32 v203, v239
	v_mfma_f32_32x32x16_f16 v[50:65], v[166:169], v[222:225], v[50:65]
	v_mfma_f32_32x32x16_f16 v[34:49], v[114:117], v[182:185], v[34:49]
	v_mov_b32_e32 v185, v239
	v_mfma_f32_32x32x16_f16 v[50:65], v[170:173], v[226:229], v[50:65]
	v_mfma_f32_32x32x16_f16 v[34:49], v[102:105], v[194:197], v[34:49]
	v_mov_b32_e32 v195, v239
	v_mov_b32_e32 v197, v239
	v_mfma_f32_32x32x16_f16 v[50:65], v[174:177], v[230:233], v[50:65]
	v_mfma_f32_32x32x16_f16 v[34:49], v[150:153], v[206:209], v[34:49]
	v_mfma_f32_32x32x16_f16 v[2:17], v[186:189], v[190:193], v[2:17]
	v_mov_b32_e32 v189, v239
	v_mov_b32_e32 v191, v239
	v_mov_b32_e32 v193, v239
	v_mfma_f32_32x32x16_f16 v[50:65], v[178:181], v[234:237], v[50:65]
	v_mfma_f32_32x32x16_f16 v[34:49], v[134:137], v[210:213], v[34:49]
	s_waitcnt vmcnt(1)
	s_nop 9
	v_add_f32_e32 v50, v244, v50
	global_store_dword v[242:243], v50, off sc1
	v_or_b32_e32 v50, 1, v240
	v_add_f32_e32 v202, v244, v51
	v_mov_b32_e32 v51, v239
	v_lshlrev_b64 v[50:51], 11, v[50:51]
	v_lshl_add_u64 v[50:51], v[0:1], 0, v[50:51]
	v_mfma_f32_32x32x16_f16 v[18:33], v[198:201], v[122:125], v[18:33]
	global_store_dword v[50:51], v202, off sc1
	v_or_b32_e32 v202, 2, v240
	v_lshlrev_b64 v[186:187], 11, v[202:203]
	v_add_f32_e32 v52, v244, v52
	v_lshl_add_u64 v[186:187], v[0:1], 0, v[186:187]
	global_store_dword v[186:187], v52, off sc1
	v_or_b32_e32 v52, 3, v240
	v_mfma_f32_32x32x16_f16 v[2:17], v[114:117], v[122:125], v[2:17]
	v_add_f32_e32 v188, v244, v53
	v_mov_b32_e32 v53, v239
	v_lshlrev_b64 v[52:53], 11, v[52:53]
	v_lshl_add_u64 v[52:53], v[0:1], 0, v[52:53]
	global_store_dword v[52:53], v188, off sc1
	v_or_b32_e32 v188, 8, v240
	v_lshlrev_b64 v[188:189], 11, v[188:189]
	v_mfma_f32_32x32x16_f16 v[34:49], v[118:121], v[214:217], v[34:49]
	v_add_f32_e32 v54, v244, v54
	v_lshl_add_u64 v[182:183], v[0:1], 0, v[188:189]
	global_store_dword v[182:183], v54, off sc1
	v_or_b32_e32 v54, 9, v240
	v_add_f32_e32 v184, v244, v55
	v_mov_b32_e32 v55, v239
	v_lshlrev_b64 v[54:55], 11, v[54:55]
	v_mfma_f32_32x32x16_f16 v[18:33], v[130:133], v[106:109], v[18:33]
	v_lshl_add_u64 v[54:55], v[0:1], 0, v[54:55]
	global_store_dword v[54:55], v184, off sc1
	v_or_b32_e32 v184, 10, v240
	v_lshlrev_b64 v[184:185], 11, v[184:185]
	v_add_f32_e32 v56, v244, v56
	v_lshl_add_u64 v[184:185], v[0:1], 0, v[184:185]
	global_store_dword v[184:185], v56, off sc1
	v_mfma_f32_32x32x16_f16 v[2:17], v[102:105], v[106:109], v[2:17]
	v_or_b32_e32 v56, 11, v240
	v_add_f32_e32 v188, v244, v57
	v_mov_b32_e32 v57, v239
	v_lshlrev_b64 v[56:57], 11, v[56:57]
	v_lshl_add_u64 v[56:57], v[0:1], 0, v[56:57]
	global_store_dword v[56:57], v188, off sc1
	v_or_b32_e32 v188, 16, v240
	v_mfma_f32_32x32x16_f16 v[34:49], v[66:69], v[218:221], v[34:49]
	v_mov_b32_e32 v189, v239
	v_lshlrev_b64 v[188:189], 11, v[188:189]
	v_add_f32_e32 v58, v244, v58
	v_lshl_add_u64 v[188:189], v[0:1], 0, v[188:189]
	global_store_dword v[188:189], v58, off sc1
	v_or_b32_e32 v58, 17, v240
	v_add_f32_e32 v190, v244, v59
	v_mfma_f32_32x32x16_f16 v[18:33], v[162:165], v[154:157], v[18:33]
	v_mov_b32_e32 v59, v239
	v_lshlrev_b64 v[58:59], 11, v[58:59]
	v_lshl_add_u64 v[58:59], v[0:1], 0, v[58:59]
	global_store_dword v[58:59], v190, off sc1
	v_or_b32_e32 v190, 18, v240
	v_lshlrev_b64 v[190:191], 11, v[190:191]
	v_add_f32_e32 v60, v244, v60
	v_mfma_f32_32x32x16_f16 v[2:17], v[150:153], v[154:157], v[2:17]
	v_lshl_add_u64 v[190:191], v[0:1], 0, v[190:191]
	global_store_dword v[190:191], v60, off sc1
	v_or_b32_e32 v60, 19, v240
	v_add_f32_e32 v192, v244, v61
	v_mov_b32_e32 v61, v239
	v_lshlrev_b64 v[60:61], 11, v[60:61]
	v_lshl_add_u64 v[60:61], v[0:1], 0, v[60:61]
	v_mfma_f32_32x32x16_f16 v[34:49], v[74:77], v[222:225], v[34:49]
	global_store_dword v[60:61], v192, off sc1
	v_or_b32_e32 v192, 24, v240
	v_lshlrev_b64 v[192:193], 11, v[192:193]
	v_add_f32_e32 v62, v244, v62
	v_lshl_add_u64 v[192:193], v[0:1], 0, v[192:193]
	global_store_dword v[192:193], v62, off sc1
	v_or_b32_e32 v62, 25, v240
	v_mfma_f32_32x32x16_f16 v[18:33], v[158:161], v[142:145], v[18:33]
	v_add_f32_e32 v194, v244, v63
	v_mov_b32_e32 v63, v239
	v_lshlrev_b64 v[62:63], 11, v[62:63]
	v_lshl_add_u64 v[62:63], v[0:1], 0, v[62:63]
	global_store_dword v[62:63], v194, off sc1
	v_or_b32_e32 v194, 26, v240
	v_lshlrev_b64 v[194:195], 11, v[194:195]
	v_mfma_f32_32x32x16_f16 v[2:17], v[134:137], v[142:145], v[2:17]
	v_add_f32_e32 v64, v244, v64
	v_lshl_add_u64 v[194:195], v[0:1], 0, v[194:195]
	global_store_dword v[194:195], v64, off sc1
	v_or_b32_e32 v64, 27, v240
	v_add_f32_e32 v196, v244, v65
	v_mov_b32_e32 v65, v239
	v_lshlrev_b64 v[64:65], 11, v[64:65]
	v_mfma_f32_32x32x16_f16 v[34:49], v[82:85], v[226:229], v[34:49]
	v_lshl_add_u64 v[64:65], v[0:1], 0, v[64:65]
	global_store_dword v[64:65], v196, off sc1
	v_or_b32_e32 v196, 32, v240
	v_lshlrev_b64 v[114:115], 11, v[196:197]
	v_lshl_add_u64 v[114:115], v[0:1], 0, v[114:115]
	v_mov_b32_e32 v117, v239
	v_mov_b32_e32 v105, v239
	v_mfma_f32_32x32x16_f16 v[18:33], v[146:149], v[126:129], v[18:33]
	v_mov_b32_e32 v107, v239
	v_mov_b32_e32 v109, v239
	v_mfma_f32_32x32x16_f16 v[2:17], v[118:121], v[126:129], v[2:17]
	v_mov_b32_e32 v119, v239
	v_mov_b32_e32 v121, v239
	v_mfma_f32_32x32x16_f16 v[34:49], v[90:93], v[230:233], v[34:49]
	v_mfma_f32_32x32x16_f16 v[18:33], v[138:141], v[70:73], v[18:33]
	v_mfma_f32_32x32x16_f16 v[2:17], v[66:69], v[70:73], v[2:17]
	v_mfma_f32_32x32x16_f16 v[34:49], v[98:101], v[234:237], v[34:49]
	v_mfma_f32_32x32x16_f16 v[18:33], v[166:169], v[78:81], v[18:33]
	s_nop 10
	v_add_f32_e32 v34, v244, v34
	global_store_dword v[114:115], v34, off sc1
	v_or_b32_e32 v34, 33, v240
	v_add_f32_e32 v116, v244, v35
	v_mov_b32_e32 v35, v239
	v_lshlrev_b64 v[34:35], 11, v[34:35]
	v_lshl_add_u64 v[34:35], v[0:1], 0, v[34:35]
	v_mfma_f32_32x32x16_f16 v[2:17], v[74:77], v[78:81], v[2:17]
	global_store_dword v[34:35], v116, off sc1
	v_or_b32_e32 v116, 34, v240
	v_lshlrev_b64 v[116:117], 11, v[116:117]
	v_add_f32_e32 v36, v244, v36
	v_lshl_add_u64 v[102:103], v[0:1], 0, v[116:117]
	global_store_dword v[102:103], v36, off sc1
	v_or_b32_e32 v36, 35, v240
	v_mfma_f32_32x32x16_f16 v[18:33], v[170:173], v[86:89], v[18:33]
	v_add_f32_e32 v104, v244, v37
	v_mov_b32_e32 v37, v239
	v_lshlrev_b64 v[36:37], 11, v[36:37]
	v_lshl_add_u64 v[36:37], v[0:1], 0, v[36:37]
	global_store_dword v[36:37], v104, off sc1
	v_or_b32_e32 v104, 40, v240
	v_lshlrev_b64 v[104:105], 11, v[104:105]
	v_mfma_f32_32x32x16_f16 v[2:17], v[82:85], v[86:89], v[2:17]
	v_add_f32_e32 v38, v244, v38
	v_lshl_add_u64 v[104:105], v[0:1], 0, v[104:105]
	global_store_dword v[104:105], v38, off sc1
	v_or_b32_e32 v38, 41, v240
	v_add_f32_e32 v106, v244, v39
	v_mov_b32_e32 v39, v239
	v_lshlrev_b64 v[38:39], 11, v[38:39]
	v_mfma_f32_32x32x16_f16 v[18:33], v[174:177], v[94:97], v[18:33]
	v_lshl_add_u64 v[38:39], v[0:1], 0, v[38:39]
	global_store_dword v[38:39], v106, off sc1
	v_or_b32_e32 v106, 42, v240
	v_lshlrev_b64 v[106:107], 11, v[106:107]
	v_add_f32_e32 v40, v244, v40
	v_lshl_add_u64 v[106:107], v[0:1], 0, v[106:107]
	global_store_dword v[106:107], v40, off sc1
	v_mfma_f32_32x32x16_f16 v[2:17], v[90:93], v[94:97], v[2:17]
	v_or_b32_e32 v40, 43, v240
	v_add_f32_e32 v108, v244, v41
	v_mov_b32_e32 v41, v239
	v_lshlrev_b64 v[40:41], 11, v[40:41]
	v_lshl_add_u64 v[40:41], v[0:1], 0, v[40:41]
	global_store_dword v[40:41], v108, off sc1
	v_or_b32_e32 v108, 48, v240
	v_mfma_f32_32x32x16_f16 v[18:33], v[178:181], v[110:113], v[18:33]
	v_lshlrev_b64 v[108:109], 11, v[108:109]
	v_add_f32_e32 v42, v244, v42
	v_lshl_add_u64 v[108:109], v[0:1], 0, v[108:109]
	global_store_dword v[108:109], v42, off sc1
	v_or_b32_e32 v42, 49, v240
	v_add_f32_e32 v116, v244, v43
	v_mov_b32_e32 v43, v239
	v_mfma_f32_32x32x16_f16 v[2:17], v[98:101], v[110:113], v[2:17]
	v_lshlrev_b64 v[42:43], 11, v[42:43]
	v_lshl_add_u64 v[42:43], v[0:1], 0, v[42:43]
	global_store_dword v[42:43], v116, off sc1
	v_or_b32_e32 v116, 50, v240
	v_mov_b32_e32 v117, v239
	v_lshlrev_b64 v[116:117], 11, v[116:117]
	s_waitcnt vmcnt(26)
	v_add_f32_e32 v18, v245, v18
	s_nop 3
	v_add_f32_e32 v2, v245, v2
	v_add_f32_e32 v44, v244, v44
	v_lshl_add_u64 v[116:117], v[0:1], 0, v[116:117]
	global_store_dword v[242:243], v18, off offset:128 sc1
	v_add_f32_e32 v18, v245, v19
	global_store_dword v[114:115], v2, off offset:128 sc1
	v_add_f32_e32 v2, v245, v3
	global_store_dword v[116:117], v44, off sc1
	v_or_b32_e32 v44, 51, v240
	v_add_f32_e32 v118, v244, v45
	v_mov_b32_e32 v45, v239
	global_store_dword v[50:51], v18, off offset:128 sc1
	v_add_f32_e32 v18, v245, v20
	global_store_dword v[34:35], v2, off offset:128 sc1
	v_add_f32_e32 v2, v245, v4
	v_lshlrev_b64 v[44:45], 11, v[44:45]
	global_store_dword v[186:187], v18, off offset:128 sc1
	v_add_f32_e32 v18, v245, v21
	global_store_dword v[102:103], v2, off offset:128 sc1
	v_add_f32_e32 v2, v245, v5
	v_lshl_add_u64 v[44:45], v[0:1], 0, v[44:45]
	global_store_dword v[52:53], v18, off offset:128 sc1
	v_add_f32_e32 v18, v245, v22
	global_store_dword v[36:37], v2, off offset:128 sc1
	v_add_f32_e32 v2, v245, v6
	global_store_dword v[44:45], v118, off sc1
	v_or_b32_e32 v118, 56, v240
	global_store_dword v[182:183], v18, off offset:128 sc1
	v_add_f32_e32 v18, v245, v23
	global_store_dword v[104:105], v2, off offset:128 sc1
	v_add_f32_e32 v2, v245, v7
	v_lshlrev_b64 v[118:119], 11, v[118:119]
	global_store_dword v[54:55], v18, off offset:128 sc1
	v_add_f32_e32 v18, v245, v24
	global_store_dword v[38:39], v2, off offset:128 sc1
	v_add_f32_e32 v2, v245, v8
	v_add_f32_e32 v46, v244, v46
	v_lshl_add_u64 v[118:119], v[0:1], 0, v[118:119]
	global_store_dword v[184:185], v18, off offset:128 sc1
	v_add_f32_e32 v18, v245, v25
	global_store_dword v[106:107], v2, off offset:128 sc1
	v_add_f32_e32 v2, v245, v9
	global_store_dword v[118:119], v46, off sc1
	v_or_b32_e32 v46, 57, v240
	v_add_f32_e32 v120, v244, v47
	v_mov_b32_e32 v47, v239
	global_store_dword v[56:57], v18, off offset:128 sc1
	v_add_f32_e32 v18, v245, v26
	global_store_dword v[40:41], v2, off offset:128 sc1
	v_add_f32_e32 v2, v245, v10
	v_lshlrev_b64 v[46:47], 11, v[46:47]
	global_store_dword v[188:189], v18, off offset:128 sc1
	v_add_f32_e32 v18, v245, v27
	global_store_dword v[108:109], v2, off offset:128 sc1
	v_add_f32_e32 v2, v245, v11
	v_lshl_add_u64 v[46:47], v[0:1], 0, v[46:47]
	global_store_dword v[58:59], v18, off offset:128 sc1
	v_add_f32_e32 v18, v245, v28
	global_store_dword v[42:43], v2, off offset:128 sc1
	v_add_f32_e32 v2, v245, v12
	global_store_dword v[46:47], v120, off sc1
	v_or_b32_e32 v120, 58, v240
	global_store_dword v[190:191], v18, off offset:128 sc1
	v_add_f32_e32 v18, v245, v29
	global_store_dword v[116:117], v2, off offset:128 sc1
	v_add_f32_e32 v2, v245, v13
	v_lshlrev_b64 v[120:121], 11, v[120:121]
	global_store_dword v[60:61], v18, off offset:128 sc1
	v_add_f32_e32 v18, v245, v30
	global_store_dword v[44:45], v2, off offset:128 sc1
	v_add_f32_e32 v2, v245, v14
	v_add_f32_e32 v48, v244, v48
	v_lshl_add_u64 v[120:121], v[0:1], 0, v[120:121]
	global_store_dword v[192:193], v18, off offset:128 sc1
	v_add_f32_e32 v18, v245, v31
	global_store_dword v[118:119], v2, off offset:128 sc1
	v_add_f32_e32 v2, v245, v15
	global_store_dword v[120:121], v48, off sc1
	v_add_f32_e32 v122, v244, v49
	v_lshlrev_b64 v[48:49], 11, v[238:239]
	global_store_dword v[62:63], v18, off offset:128 sc1
	v_add_f32_e32 v18, v245, v32
	global_store_dword v[46:47], v2, off offset:128 sc1
	v_add_f32_e32 v2, v245, v16
	v_lshl_add_u64 v[0:1], v[0:1], 0, v[48:49]
	global_store_dword v[194:195], v18, off offset:128 sc1
	v_add_f32_e32 v18, v245, v33
	global_store_dword v[120:121], v2, off offset:128 sc1
	v_add_f32_e32 v2, v245, v17
	global_store_dword v[0:1], v122, off sc1
	global_store_dword v[64:65], v18, off offset:128 sc1
	global_store_dword v[0:1], v2, off offset:128 sc1
	s_endpgm
	.p2align	8

.LBB3_30:
	v_add_f32_e32 v32, v48, v49
	v_add_f32_e32 v32, v50, v32
	v_add_f32_e32 v32, v51, v32
	v_add_f32_e32 v32, v52, v32
	v_add_f32_e32 v32, v53, v32
	v_add_f32_e32 v32, v54, v32
	v_add_f32_e32 v32, v55, v32
	v_add_f32_e32 v32, v56, v32
	v_add_f32_e32 v32, v57, v32
	v_add_f32_e32 v32, v58, v32
	v_add_f32_e32 v32, v59, v32
	v_add_f32_e32 v32, v60, v32
	v_add_f32_e32 v32, v61, v32
	v_add_f32_e32 v32, v62, v32
	v_add_f32_e32 v32, v63, v32
	v_add_f32_e32 v32, v80, v32
	v_add_f32_e32 v32, v81, v32
	v_add_f32_e32 v32, v82, v32
	v_add_f32_e32 v32, v83, v32
	v_add_f32_e32 v32, v84, v32
	v_add_f32_e32 v32, v85, v32
	v_add_f32_e32 v32, v86, v32
	v_add_f32_e32 v32, v87, v32
	v_add_f32_e32 v32, v88, v32
	v_add_f32_e32 v32, v89, v32
	v_add_f32_e32 v32, v90, v32
	v_add_f32_e32 v32, v91, v32
	v_add_f32_e32 v32, v92, v32
	s_cmp_lg_u32 0, -1
	v_add_f32_e32 v32, v93, v32
	s_cselect_b32 s0, 0, 0
	v_add_f32_e32 v32, v94, v32
	s_addk_i32 s0, 0x6000
	v_add_f32_e32 v32, v95, v32
	v_add3_u32 v33, v203, s0, v204
	v_add_f32_e32 v32, v64, v32
	v_cvt_pk_f16_f32 v34, v48, v49
	v_cvt_pk_f16_f32 v35, v50, v51
	v_cvt_pk_f16_f32 v36, v52, v53
	v_cvt_pk_f16_f32 v37, v54, v55
	v_cvt_pk_f16_f32 v38, v56, v57
	v_cvt_pk_f16_f32 v39, v58, v59
	v_cvt_pk_f16_f32 v40, v60, v61
	v_cvt_pk_f16_f32 v41, v62, v63
	v_cvt_pk_f16_f32 v42, v80, v81
	v_cvt_pk_f16_f32 v43, v82, v83
	v_cvt_pk_f16_f32 v44, v84, v85
	v_cvt_pk_f16_f32 v45, v86, v87
	v_cvt_pk_f16_f32 v46, v88, v89
	v_cvt_pk_f16_f32 v47, v90, v91
	v_cvt_pk_f16_f32 v48, v92, v93
	v_cvt_pk_f16_f32 v49, v94, v95
	v_add3_u32 v33, v33, v202, s90
	ds_read_b64_tr_b16 v[50:51],v33 offset:0
	ds_read_b64_tr_b16 v[52:53],v33 offset:512
	ds_read_b64_tr_b16 v[54:55],v33 offset:1024
	ds_read_b64_tr_b16 v[56:57],v33 offset:1536
	ds_read_b64_tr_b16 v[58:59],v33 offset:2048
	ds_read_b64_tr_b16 v[60:61],v33 offset:2560
	ds_read_b64_tr_b16 v[62:63],v33 offset:3072
	ds_read_b64_tr_b16 v[64:65],v33 offset:3584
	s_waitcnt lgkmcnt(0)
	s_nop 0
	v_mfma_f32_32x32x16_f16 v[0:15], v[34:37], v[50:53], v[0:15]
	ds_read_b64_tr_b16 v[50:51],v33 offset:4096
	ds_read_b64_tr_b16 v[52:53],v33 offset:4608
	v_mfma_f32_32x32x16_f16 v[0:15], v[38:41], v[54:57], v[0:15]
	ds_read_b64_tr_b16 v[54:55],v33 offset:5120
	ds_read_b64_tr_b16 v[56:57],v33 offset:5632
	v_mfma_f32_32x32x16_f16 v[0:15], v[42:45], v[58:61], v[0:15]
	ds_read_b64_tr_b16 v[58:59],v33 offset:6144
	ds_read_b64_tr_b16 v[60:61],v33 offset:6656
	ds_read_b64_tr_b16 v[66:67],v33 offset:7168
	ds_read_b64_tr_b16 v[68:69],v33 offset:7680
	s_waitcnt lgkmcnt(0)
	v_mfma_f32_32x32x16_f16 v[0:15], v[46:49], v[62:65], v[0:15]
	v_mfma_f32_32x32x16_f16 v[16:31], v[34:37], v[50:53], v[16:31]
	s_waitcnt vmcnt(0)
	v_mov_b32_e32 v33, v32
	s_nop 1
	v_permlane32_swap_b32_e32 v32, v33
	v_cmp_gt_u32_e32 vcc, 32, v198
	v_mfma_f32_32x32x16_f16 v[16:31], v[38:41], v[54:57], v[16:31]
	v_mfma_f32_32x32x16_f16 v[16:31], v[42:45], v[58:61], v[16:31]
	v_mfma_f32_32x32x16_f16 v[16:31], v[46:49], v[66:69], v[16:31]
	s_and_saveexec_b64 s[0:1], vcc
	v_add_f32_e32 v32, v32, v33
	ds_write_b32 v197, v32 offset:49280
	s_or_b64 exec, exec, s[0:1]
	s_waitcnt lgkmcnt(0)
	v_lshl_add_u32 v40, v200, 4, s84
	ds_read_b128 v[32:35], v40 offset:49280
	ds_read_b128 v[36:39], v40 offset:49312
	s_lshl_b32 s2, s83, 8
	s_lshl_b64 s[0:1], s[68:69], 11
	s_or_b32 s0, s0, s2
	s_waitcnt lgkmcnt(0)
	v_rcp_f32_e32 v41, v32
	s_lshl_b32 s2, s82, 5
	s_add_u32 s0, s0, s2
	v_rcp_f32_e32 v42, v33
	s_addc_u32 s1, s1, 0
	s_lshl_b32 s2, s82, 12
	v_rcp_f32_e32 v43, v34
	v_rcp_f32_e32 v44, v35
	v_rcp_f32_e32 v45, v36
	ds_read_b128 v[32:35], v40 offset:49344
	v_rcp_f32_e32 v46, v37
	v_rcp_f32_e32 v47, v38
	v_rcp_f32_e32 v48, v39
	ds_read_b128 v[36:39], v40 offset:49376
	s_add_i32 s2, s2, 0
	v_lshlrev_b32_e32 v40, 1, v199
	v_add3_u32 v40, s2, v196, v40
	v_fma_mixlo_f16 v0, v0, v41, 0
	ds_write_b16 v40, v0 offset:51200
	v_fma_mixlo_f16 v0, v16, v41, 0
	ds_write_b16 v40, v0 offset:51264
	v_fma_mixlo_f16 v0, v1, v42, 0
	ds_write_b16 v40, v0 offset:51328
	v_fma_mixlo_f16 v0, v17, v42, 0
	ds_write_b16 v40, v0 offset:51392
	v_fma_mixlo_f16 v0, v2, v43, 0
	ds_write_b16 v40, v0 offset:51456
	v_fma_mixlo_f16 v0, v18, v43, 0
	ds_write_b16 v40, v0 offset:51520
	v_fma_mixlo_f16 v0, v3, v44, 0
	ds_write_b16 v40, v0 offset:51584
	v_fma_mixlo_f16 v0, v19, v44, 0
	ds_write_b16 v40, v0 offset:51648
	v_fma_mixlo_f16 v0, v4, v45, 0
	ds_write_b16 v40, v0 offset:52224
	v_fma_mixlo_f16 v0, v20, v45, 0
	ds_write_b16 v40, v0 offset:52288
	v_fma_mixlo_f16 v0, v5, v46, 0
	ds_write_b16 v40, v0 offset:52352
	v_fma_mixlo_f16 v0, v21, v46, 0
	s_waitcnt lgkmcnt(12)
	v_rcp_f32_e32 v32, v32
	ds_write_b16 v40, v0 offset:52416
	v_fma_mixlo_f16 v0, v6, v47, 0
	ds_write_b16 v40, v0 offset:52480
	v_fma_mixlo_f16 v0, v22, v47, 0
	v_rcp_f32_e32 v33, v33
	ds_write_b16 v40, v0 offset:52544
	v_fma_mixlo_f16 v0, v7, v48, 0
	ds_write_b16 v40, v0 offset:52608
	v_fma_mixlo_f16 v0, v23, v48, 0
	v_rcp_f32_e32 v34, v34
	ds_write_b16 v40, v0 offset:52672
	v_fma_mixlo_f16 v0, v8, v32, 0
	ds_write_b16 v40, v0 offset:53248
	v_fma_mixlo_f16 v0, v24, v32, 0
	v_rcp_f32_e32 v35, v35
	ds_write_b16 v40, v0 offset:53312
	v_fma_mixlo_f16 v0, v9, v33, 0
	ds_write_b16 v40, v0 offset:53376
	v_fma_mixlo_f16 v0, v25, v33, 0
	s_waitcnt lgkmcnt(14)
	v_rcp_f32_e32 v36, v36
	ds_write_b16 v40, v0 offset:53440
	v_fma_mixlo_f16 v0, v10, v34, 0
	ds_write_b16 v40, v0 offset:53504
	v_fma_mixlo_f16 v0, v26, v34, 0
	v_rcp_f32_e32 v37, v37
	ds_write_b16 v40, v0 offset:53568
	v_fma_mixlo_f16 v0, v11, v35, 0
	ds_write_b16 v40, v0 offset:53632
	v_fma_mixlo_f16 v0, v27, v35, 0
	v_rcp_f32_e32 v38, v38
	ds_write_b16 v40, v0 offset:53696
	v_fma_mixlo_f16 v0, v12, v36, 0
	ds_write_b16 v40, v0 offset:54272
	v_fma_mixlo_f16 v0, v28, v36, 0
	v_rcp_f32_e32 v39, v39
	ds_write_b16 v40, v0 offset:54336
	v_fma_mixlo_f16 v0, v13, v37, 0
	ds_write_b16 v40, v0 offset:54400
	v_fma_mixlo_f16 v0, v29, v37, 0
	ds_write_b16 v40, v0 offset:54464
	v_fma_mixlo_f16 v0, v14, v38, 0
	ds_write_b16 v40, v0 offset:54528
	v_fma_mixlo_f16 v0, v30, v38, 0
	ds_write_b16 v40, v0 offset:54592
	v_fma_mixlo_f16 v0, v15, v39, 0
	ds_write_b16 v40, v0 offset:54656
	v_fma_mixlo_f16 v0, v31, v39, 0
	ds_write_b16 v40, v0 offset:54720
	v_and_b32_e32 v0, 56, v201
	v_lshlrev_b32_e32 v8, 1, v0
	s_lshl_b64 s[0:1], s[0:1], 10
	v_lshrrev_b32_e32 v14, 3, v198
	v_add_u32_e32 v15, s2, v8
	s_add_u32 s0, s70, s0
	s_waitcnt lgkmcnt(0)
	v_lshl_add_u32 v0, v14, 7, v15
	v_or_b32_e32 v16, 8, v14
	s_addc_u32 s1, s71, s1
	s_lshl_b32 s3, s33, 7
	ds_read_b128 v[0:3], v0 offset:51200
	v_lshl_add_u32 v4, v16, 7, v15
	s_add_u32 s0, s0, s3
	ds_read_b128 v[4:7], v4 offset:51200
	s_addc_u32 s1, s1, 0
	v_mov_b32_e32 v9, 0
	v_lshl_add_u64 v[10:11], s[0:1], 0, v[8:9]
	v_lshlrev_b32_e32 v8, 10, v14
	v_lshl_add_u64 v[12:13], v[10:11], 0, v[8:9]
	v_lshlrev_b32_e32 v8, 10, v16
	s_waitcnt lgkmcnt(1)
	global_store_dwordx4 v[12:13], v[0:3], off sc1
	s_nop 1
	v_lshl_add_u64 v[0:1], v[10:11], 0, v[8:9]
	s_waitcnt lgkmcnt(0)
	global_store_dwordx4 v[0:1], v[4:7], off sc1
	s_nop 1
	v_or_b32_e32 v4, 16, v14
	v_lshl_add_u32 v0, v4, 7, v15
	v_or_b32_e32 v14, 24, v14
	ds_read_b128 v[0:3], v0 offset:51200
	v_lshlrev_b32_e32 v8, 10, v4
	v_lshl_add_u32 v4, v14, 7, v15
	ds_read_b128 v[4:7], v4 offset:51200
	v_lshl_add_u64 v[12:13], v[10:11], 0, v[8:9]
	v_lshlrev_b32_e32 v8, 10, v14
	s_waitcnt lgkmcnt(1)
	global_store_dwordx4 v[12:13], v[0:3], off sc1
	s_nop 1
	v_lshl_add_u64 v[0:1], v[10:11], 0, v[8:9]
	s_waitcnt lgkmcnt(0)
	global_store_dwordx4 v[0:1], v[4:7], off sc1
	s_waitcnt lgkmcnt(0)
	s_barrier
	s_endpgm
.LBB3_33:
	v_max_f32_e32 v65, v65, v65
	v_max_f32_e32 v65, 0, v65
	v_add_f32_e32 v66, v206, v65
	v_sub_f32_e32 v63, v63, v65
	v_sub_f32_e32 v62, v62, v65
	v_sub_f32_e32 v61, v61, v65
	v_sub_f32_e32 v60, v60, v65
	v_sub_f32_e32 v59, v59, v65
	v_sub_f32_e32 v58, v58, v65
	v_sub_f32_e32 v57, v57, v65
	v_sub_f32_e32 v56, v56, v65
	v_sub_f32_e32 v55, v55, v65
	v_sub_f32_e32 v54, v54, v65
	v_sub_f32_e32 v53, v53, v65
	v_sub_f32_e32 v52, v52, v65
	v_sub_f32_e32 v51, v51, v65
	v_sub_f32_e32 v50, v50, v65
	v_sub_f32_e32 v49, v49, v65
	v_sub_f32_e32 v48, v48, v65
	v_sub_f32_e32 v47, v47, v65
	v_sub_f32_e32 v46, v46, v65
	v_sub_f32_e32 v45, v45, v65
	v_sub_f32_e32 v44, v44, v65
	v_sub_f32_e32 v43, v43, v65
	v_sub_f32_e32 v42, v42, v65
	v_sub_f32_e32 v41, v41, v65
	v_sub_f32_e32 v40, v40, v65
	v_sub_f32_e32 v39, v39, v65
	v_sub_f32_e32 v38, v38, v65
	v_sub_f32_e32 v37, v37, v65
	v_sub_f32_e32 v36, v36, v65
	v_sub_f32_e32 v35, v35, v65
	v_sub_f32_e32 v34, v34, v65
	v_sub_f32_e32 v33, v33, v65
	v_sub_f32_e32 v32, v32, v65
	v_exp_f32_e64 v65, -v65
	v_xor_b32_e32 v66, 0x80000000, v66
	v_mov_b32_e32 v67, v66
	v_mov_b32_e32 v68, v66
	v_mov_b32_e32 v69, v66
	v_mov_b32_e32 v70, v66
	v_mov_b32_e32 v71, v66
	v_mov_b32_e32 v72, v66
	v_mov_b32_e32 v73, v66
	v_mov_b32_e32 v74, v66
	v_mov_b32_e32 v75, v66
	v_mov_b32_e32 v76, v66
	v_mov_b32_e32 v77, v66
	v_mov_b32_e32 v78, v66
	v_mov_b32_e32 v79, v66
	v_mov_b32_e32 v80, v66
	v_mov_b32_e32 v81, v66
	v_cmp_gt_u32_e32 vcc, 32, v198
	s_and_saveexec_b64 s[2:3], vcc
	ds_write_b32 v197, v65 offset:49152
	s_or_b64 exec, exec, s[2:3]
	v_mul_f32_e32 v64, v64, v65
	s_branch .LBB3_28
	.p2align	8
